# speedup vs baseline: 1.0008x; 1.0008x over previous
_Z12final_kernelPKDv4_fS1_PKfS3_Pf:
	s_load_dwordx4 s[4:7], s[0:1], 0x0
	s_load_dwordx2 s[2:3], s[0:1], 0x10
	s_load_dwordx2 s[8:9], s[0:1], 0x20
	v_and_b32_e32 v1, 0x1ff, v0
	v_readfirstlane_b32 s10, v0
	v_lshlrev_b32_e32 v3, 2, v1
	v_add_u32_e32 v4, 0x1000, v3
	v_add_u32_e32 v5, 0x2000, v3
	v_add_u32_e32 v6, 0x3000, v3
	v_add_u32_e32 v7, 0x4000, v3
	v_add_u32_e32 v8, 0x5000, v3
	v_add_u32_e32 v9, 0x6000, v3
	v_add_u32_e32 v10, 0x7000, v3
	s_cmpk_ge_u32 s10, 0x200
	s_waitcnt lgkmcnt(0)
	s_cselect_b32 s4, s6, s4
	s_cselect_b32 s5, s7, s5
	global_load_dword v12, v3, s[4:5]
	global_load_dword v13, v3, s[4:5] offset:2048
	global_load_dword v14, v4, s[4:5]
	global_load_dword v15, v4, s[4:5] offset:2048
	global_load_dword v16, v5, s[4:5]
	global_load_dword v17, v5, s[4:5] offset:2048
	global_load_dword v18, v6, s[4:5]
	global_load_dword v19, v6, s[4:5] offset:2048
	global_load_dword v20, v7, s[4:5]
	global_load_dword v21, v7, s[4:5] offset:2048
	global_load_dword v22, v8, s[4:5]
	global_load_dword v23, v8, s[4:5] offset:2048
	global_load_dword v24, v9, s[4:5]
	global_load_dword v25, v9, s[4:5] offset:2048
	global_load_dword v26, v10, s[4:5]
	global_load_dword v27, v10, s[4:5] offset:2048
	global_load_dword v44, v3, s[2:3]
	global_load_dword v45, v3, s[2:3] offset:2048
	s_waitcnt vmcnt(2)
	v_max3_f32 v46, v12, v13, v14
	v_max3_f32 v47, v15, v16, v17
	v_max3_f32 v48, v18, v19, v20
	v_max3_f32 v49, v21, v22, v23
	v_max3_f32 v46, v46, v24, v25
	v_max3_f32 v47, v47, v26, v27
	v_max3_f32 v46, v46, v48, v49
	v_max_f32_e32 v46, v46, v47
	v_sub_f32_e32 v12, v12, v46
	v_sub_f32_e32 v13, v13, v46
	v_sub_f32_e32 v14, v14, v46
	v_sub_f32_e32 v15, v15, v46
	v_sub_f32_e32 v16, v16, v46
	v_sub_f32_e32 v17, v17, v46
	v_sub_f32_e32 v18, v18, v46
	v_sub_f32_e32 v19, v19, v46
	v_sub_f32_e32 v20, v20, v46
	v_sub_f32_e32 v21, v21, v46
	v_sub_f32_e32 v22, v22, v46
	v_sub_f32_e32 v23, v23, v46
	v_sub_f32_e32 v24, v24, v46
	v_sub_f32_e32 v25, v25, v46
	v_sub_f32_e32 v26, v26, v46
	v_sub_f32_e32 v27, v27, v46
	v_exp_f32_e32 v12, v12
	v_exp_f32_e32 v13, v13
	v_exp_f32_e32 v14, v14
	v_exp_f32_e32 v15, v15
	v_exp_f32_e32 v16, v16
	v_exp_f32_e32 v17, v17
	v_exp_f32_e32 v18, v18
	v_exp_f32_e32 v19, v19
	v_exp_f32_e32 v20, v20
	v_exp_f32_e32 v21, v21
	v_exp_f32_e32 v22, v22
	v_exp_f32_e32 v23, v23
	v_exp_f32_e32 v24, v24
	v_exp_f32_e32 v25, v25
	v_exp_f32_e32 v26, v26
	v_exp_f32_e32 v27, v27
	s_nop 0
	v_add_f32_e32 v12, v12, v20
	v_add_f32_e32 v13, v13, v21
	v_add_f32_e32 v14, v14, v22
	v_add_f32_e32 v15, v15, v23
	v_add_f32_e32 v16, v16, v24
	v_add_f32_e32 v17, v17, v25
	v_add_f32_e32 v18, v18, v26
	v_add_f32_e32 v19, v19, v27
	v_add_f32_e32 v12, v12, v16
	v_add_f32_e32 v13, v13, v17
	v_add_f32_e32 v14, v14, v18
	v_add_f32_e32 v15, v15, v19
	v_add_f32_e32 v12, v12, v14
	v_add_f32_e32 v13, v13, v15
	v_add_f32_e32 v47, v12, v13
	v_log_f32_e32 v47, v47
	s_mov_b32 s11, 0x3f317217
	v_add_f32_e32 v47, v46, v47
	v_mul_f32_e32 v48, 0x3f317217, v47
	v_fma_f32 v48, v47, s11, -v48
	v_fmamk_f32 v48, v47, 0x3377d1cf, v48
	v_fmac_f32_e32 v48, 0x3f317217, v47
	v_mov_b32_e32 v46, v48
	s_waitcnt vmcnt(0)
	v_sub_f32_e32 v46, v46, v44
	v_cmp_lt_f32_e32 vcc, 0, v45
	s_nop 1
	v_cndmask_b32_e32 v46, 0, v46, vcc
	v_cmp_lt_f32_e32 vcc, 0, v46
	v_max_f32_e32 v2, 0, v46
	s_nop 0
	v_cndmask_b32_e64 v3, 0, 1.0, vcc
	s_nop 0
	s_nop 0
	v_add_f32_dpp v2, v2, v2 quad_perm:[1,0,3,2] row_mask:0xf bank_mask:0xf
	v_add_f32_dpp v3, v3, v3 quad_perm:[1,0,3,2] row_mask:0xf bank_mask:0xf
	s_nop 0
	v_add_f32_dpp v2, v2, v2 quad_perm:[2,3,0,1] row_mask:0xf bank_mask:0xf
	v_add_f32_dpp v3, v3, v3 quad_perm:[2,3,0,1] row_mask:0xf bank_mask:0xf
	s_nop 0
	v_add_f32_dpp v2, v2, v2 row_half_mirror row_mask:0xf bank_mask:0xf
	v_add_f32_dpp v3, v3, v3 row_half_mirror row_mask:0xf bank_mask:0xf
	s_nop 0
	v_add_f32_dpp v2, v2, v2 row_mirror row_mask:0xf bank_mask:0xf
	v_add_f32_dpp v3, v3, v3 row_mirror row_mask:0xf bank_mask:0xf
	s_nop 0
	v_add_f32_dpp v2, v2, v2 row_bcast:15 row_mask:0xa bank_mask:0xf
	v_add_f32_dpp v3, v3, v3 row_bcast:15 row_mask:0xa bank_mask:0xf
	s_nop 0
	v_add_f32_dpp v2, v2, v2 row_bcast:31 row_mask:0xc bank_mask:0xf
	v_add_f32_dpp v3, v3, v3 row_bcast:31 row_mask:0xc bank_mask:0xf
	s_nop 1
	v_readlane_b32 s12, v2, 63
	v_readlane_b32 s13, v3, 63
	s_lshr_b32 s10, s10, 6
	s_lshl_b32 s10, s10, 2
	v_mov_b32_e32 v4, s10
	v_mov_b32_e32 v5, s12
	v_mov_b32_e32 v6, s13
	ds_write2_b32 v4, v5, v6 offset1:16
	s_waitcnt lgkmcnt(0)
	s_barrier
	s_cmp_lg_u32 s10, 0
	s_cbranch_scc1 .Lfin_end
	v_and_b32_e32 v4, 15, v0
	v_lshlrev_b32_e32 v4, 2, v4
	ds_read2_b32 v[2:3], v4 offset1:16
	s_waitcnt lgkmcnt(0)
	s_nop 0
	s_nop 0
	v_add_f32_dpp v2, v2, v2 quad_perm:[1,0,3,2] row_mask:0xf bank_mask:0xf
	v_add_f32_dpp v3, v3, v3 quad_perm:[1,0,3,2] row_mask:0xf bank_mask:0xf
	s_nop 0
	v_add_f32_dpp v2, v2, v2 quad_perm:[2,3,0,1] row_mask:0xf bank_mask:0xf
	v_add_f32_dpp v3, v3, v3 quad_perm:[2,3,0,1] row_mask:0xf bank_mask:0xf
	s_nop 0
	v_add_f32_dpp v2, v2, v2 row_half_mirror row_mask:0xf bank_mask:0xf
	v_add_f32_dpp v3, v3, v3 row_half_mirror row_mask:0xf bank_mask:0xf
	v_max_f32_e32 v5, 1.0, v3
	v_div_scale_f32 v6, s[12:13], v5, v5, v2
	v_rcp_f32_e32 v7, v6
	v_div_scale_f32 v8, vcc, v2, v5, v2
	v_fma_f32 v9, -v6, v7, 1.0
	v_fmac_f32_e32 v7, v9, v7
	v_mul_f32_e32 v9, v8, v7
	v_fma_f32 v10, -v6, v9, v8
	v_fmac_f32_e32 v9, v10, v7
	v_fma_f32 v6, -v6, v9, v8
	v_div_fmas_f32 v6, v6, v7, v9
	v_div_fixup_f32 v6, v6, v5, v2
	v_cmp_lt_f32_e32 vcc, 0, v3
	s_nop 1
	v_cndmask_b32_e32 v6, 0, v6, vcc
	s_nop 1
	v_add_f32_dpp v7, v6, v6 row_shl:8 row_mask:0xf bank_mask:0xf
	v_mov_b32_e32 v8, 0
	v_mul_f32_e32 v7, 0.5, v7
	v_cmp_eq_u32_e32 vcc, 0, v0
	s_and_saveexec_b64 s[12:13], vcc
	global_store_dword v8, v7, s[8:9]
